# baseline (speedup 1.0000x reference)
.LBB3_19:
	s_or_b64 exec, exec, s[8:9]
	s_lshl_b32 s22, s3, 3
	s_and_b32 s8, s20, 64
	s_and_b32 s9, s22, 56
	s_or_b32 s8, s8, s9
	s_waitcnt lgkmcnt(0)
	s_lshl_b32 s6, s6, 1
	s_lshl_b32 s23, s8, 7
	s_ashr_i32 s9, s6, 31
	s_add_u32 s8, s6, s23
	s_addc_u32 s9, s9, 0
	s_lshl_b64 s[8:9], s[8:9], 8
	s_add_u32 s6, s4, s8
	s_addc_u32 s8, s5, s9
	s_lshl_b32 s4, s7, 1
	s_ashr_i32 s5, s4, 31
	v_mul_u32_u24_e32 v1, 0x1112, v0
	s_lshl_b64 s[4:5], s[4:5], 1
	v_lshrrev_b32_e32 v34, 16, v1
	s_add_u32 s6, s6, s4
	v_mad_i32_i24 v8, v34, -15, v0
	v_mov_b32_e32 v1, 0x1c00
	v_mov_b32_e32 v4, 0x1d00
	v_cmp_lt_u32_e32 vcc, 14, v0
	s_addc_u32 s7, s8, s5
	s_waitcnt vmcnt(0)
	v_lshlrev_b32_e32 v2, 1, v8
	v_cndmask_b32_e32 v4, v1, v4, vcc
	v_mov_b32_e32 v5, 0
	v_ashrrev_i32_e32 v3, 31, v2
	v_lshl_add_u64 v[6:7], s[6:7], 0, v[4:5]
	v_lshl_add_u64 v[6:7], v[2:3], 1, v[6:7]
	v_add_co_u32_e32 v6, vcc, 0x38000, v6
	s_movk_i32 s4, 0xff
	s_nop 0
	v_addc_co_u32_e32 v7, vcc, 0, v7, vcc
	global_load_dword v1, v[6:7], off
	v_lshlrev_b32_e32 v27, 2, v8
	v_cmp_gt_u32_e32 vcc, s4, v0
	v_mad_u32_u24 v26, v34, 60, v27
	s_and_saveexec_b64 s[4:5], vcc
	s_cbranch_execz .LBB3_21
	v_lshl_add_u32 v23, v34, 8, v27
	v_add_u32_e32 v24, 0x6200, v23
	v_add_u32_e32 v25, 4, v26
	v_cmp_le_u32_e64 s[8:9], 13, v34
	v_cmp_le_u32_e64 s[10:11], 9, v34
	v_cmp_le_u32_e64 s[12:13], 5, v34
	v_cmp_le_u32_e64 s[14:15], 1, v34
	v_cmp_le_u32_e64 s[16:17], 14, v34
	v_cmp_le_u32_e64 s[18:19], 10, v34
	v_cmp_le_u32_e64 s[24:25], 6, v34
	global_load_dword v9, v23, s[6:7]
	v_cndmask_b32_e64 v2, v23, v24, s[8:9]
	v_add_u32_e32 v3, 0x1100, v2
	global_load_dword v10, v3, s[6:7]
	v_add_u32_e32 v3, 0x8400, v23
	global_load_dword v11, v3, s[6:7]
	v_cndmask_b32_e64 v2, v23, v24, s[10:11]
	v_add_u32_e32 v3, 0x9500, v2
	global_load_dword v12, v3, s[6:7]
	v_add_u32_e32 v3, 0x10800, v23
	global_load_dword v13, v3, s[6:7]
	v_cndmask_b32_e64 v2, v23, v24, s[12:13]
	v_add_u32_e32 v3, 0x11900, v2
	global_load_dword v14, v3, s[6:7]
	v_add_u32_e32 v3, 0x18c00, v23
	global_load_dword v15, v3, s[6:7]
	v_cndmask_b32_e64 v2, v23, v24, s[14:15]
	v_add_u32_e32 v3, 0x19d00, v2
	global_load_dword v16, v3, s[6:7]
	v_cndmask_b32_e64 v2, v23, v24, s[16:17]
	v_add_u32_e32 v3, 0x21000, v2
	global_load_dword v17, v3, s[6:7]
	v_add_u32_e32 v3, 0x28300, v23
	global_load_dword v18, v3, s[6:7]
	v_cndmask_b32_e64 v2, v23, v24, s[18:19]
	v_add_u32_e32 v3, 0x29400, v2
	global_load_dword v19, v3, s[6:7]
	v_add_u32_e32 v3, 0x30700, v23
	global_load_dword v20, v3, s[6:7]
	v_cndmask_b32_e64 v2, v23, v24, s[24:25]
	v_add_u32_e32 v3, 0x31800, v2
	global_load_dword v21, v3, s[6:7]
	v_add_u32_e32 v3, 0x38b00, v23
	global_load_dword v22, v3, s[6:7]
	s_waitcnt vmcnt(13)
	ds_write_b32 v26, v9 offset:4
	v_cndmask_b32_e64 v2, v26, v25, s[8:9]
	s_waitcnt vmcnt(12)
	ds_write_b32 v2, v10 offset:1024
	s_waitcnt vmcnt(11)
	ds_write_b32 v26, v11 offset:2048
	v_cndmask_b32_e64 v2, v26, v25, s[10:11]
	s_waitcnt vmcnt(10)
	ds_write_b32 v2, v12 offset:3068
	s_waitcnt vmcnt(9)
	ds_write_b32 v26, v13 offset:4092
	v_cndmask_b32_e64 v2, v26, v25, s[12:13]
	s_waitcnt vmcnt(8)
	ds_write_b32 v2, v14 offset:5112
	s_waitcnt vmcnt(7)
	ds_write_b32 v26, v15 offset:6136
	v_cndmask_b32_e64 v2, v26, v25, s[14:15]
	s_waitcnt vmcnt(6)
	ds_write_b32 v2, v16 offset:7156
	v_cndmask_b32_e64 v2, v26, v25, s[16:17]
	s_waitcnt vmcnt(5)
	ds_write_b32 v2, v17 offset:8180
	s_waitcnt vmcnt(4)
	ds_write_b32 v26, v18 offset:9204
	v_cndmask_b32_e64 v2, v26, v25, s[18:19]
	s_waitcnt vmcnt(3)
	ds_write_b32 v2, v19 offset:10224
	s_waitcnt vmcnt(2)
	ds_write_b32 v26, v20 offset:11248
	v_cndmask_b32_e64 v2, v26, v25, s[24:25]
	s_waitcnt vmcnt(1)
	ds_write_b32 v2, v21 offset:12268
	s_waitcnt vmcnt(0)
	ds_write_b32 v26, v22 offset:13292
